# MLA fast tile a: first 8 V^T fragment reads hoisted above the exp block into free registers
# speedup vs baseline: 1.0248x; 1.0011x over previous
.Lf_a:
	v_add_u32_e32 v248, s14, v151
	v_add_u32_e32 v249, s14, v152
	ds_read_b64_tr_b16 v[224:225], v248
	ds_read_b64_tr_b16 v[226:227], v249 offset:768
	ds_read_b64_tr_b16 v[228:229], v248 offset:6144
	ds_read_b64_tr_b16 v[230:231], v249 offset:6912
	ds_read_b64_tr_b16 v[232:233], v248 offset:12288
	ds_read_b64_tr_b16 v[234:235], v249 offset:13056
	ds_read_b64_tr_b16 v[236:237], v248 offset:18432
	ds_read_b64_tr_b16 v[238:239], v249 offset:19200
	v_exp_f32_e32 v80, v80
	v_exp_f32_e32 v81, v81
	v_exp_f32_e32 v82, v82
	v_exp_f32_e32 v83, v83
	v_add_f32_e32 v146, 0, v80
	v_exp_f32_e32 v84, v84
	v_add_f32_e32 v146, v81, v146
	v_exp_f32_e32 v85, v85
	v_add_f32_e32 v146, v82, v146
	v_exp_f32_e32 v86, v86
	v_add_f32_e32 v146, v83, v146
	v_exp_f32_e32 v87, v87
	v_add_f32_e32 v146, v84, v146
	v_exp_f32_e32 v88, v88
	v_add_f32_e32 v146, v85, v146
	v_exp_f32_e32 v89, v89
	v_add_f32_e32 v146, v86, v146
	v_exp_f32_e32 v90, v90
	v_add_f32_e32 v146, v87, v146
	v_exp_f32_e32 v91, v91
	v_add_f32_e32 v146, v88, v146
	v_exp_f32_e32 v92, v92
	v_add_f32_e32 v146, v89, v146
	v_exp_f32_e32 v93, v93
	v_add_f32_e32 v146, v90, v146
	v_exp_f32_e32 v94, v94
	v_add_f32_e32 v146, v91, v146
	v_exp_f32_e32 v95, v95
	v_add_f32_e32 v146, v92, v146
	v_exp_f32_e32 v64, v64
	v_add_f32_e32 v146, v93, v146
	v_exp_f32_e32 v65, v65
	v_add_f32_e32 v146, v94, v146
	v_exp_f32_e32 v66, v66
	v_add_f32_e32 v146, v95, v146
	v_exp_f32_e32 v67, v67
	v_add_f32_e32 v146, v64, v146
	v_exp_f32_e32 v68, v68
	v_add_f32_e32 v146, v65, v146
	v_exp_f32_e32 v69, v69
	v_add_f32_e32 v146, v66, v146
	v_exp_f32_e32 v70, v70
	v_add_f32_e32 v146, v67, v146
	v_exp_f32_e32 v71, v71
	v_add_f32_e32 v146, v68, v146
	v_exp_f32_e32 v161, v72
	v_add_f32_e32 v146, v69, v146
	v_add_f32_e32 v146, v70, v146
	v_add_f32_e32 v146, v71, v146
	v_add_f32_e32 v72, v161, v146
	v_exp_f32_e32 v146, v73
	v_exp_f32_e32 v162, v74
	v_exp_f32_e32 v163, v75
	v_exp_f32_e32 v164, v76
	v_add_f32_e32 v72, v146, v72
	v_exp_f32_e32 v165, v77
	v_add_f32_e32 v72, v162, v72
	v_exp_f32_e32 v166, v78
	v_add_f32_e32 v72, v163, v72
	v_exp_f32_e32 v167, v79
	v_add_f32_e32 v72, v164, v72
	v_add_f32_e32 v72, v165, v72
	v_add_f32_e32 v72, v166, v72
	v_cvt_pk_bf16_f32 v76, v80, v81
	v_cvt_pk_bf16_f32 v77, v84, v85
	v_cvt_pk_bf16_f32 v78, v82, v83
	v_cvt_pk_bf16_f32 v79, v86, v87
	v_cvt_pk_bf16_f32 v64, v64, v65
	v_cvt_pk_bf16_f32 v65, v68, v69
	v_cvt_pk_bf16_f32 v68, v161, v146
	v_add_u32_e32 v146, s14, v151
	v_add_f32_e32 v159, v167, v72
	v_cvt_pk_bf16_f32 v72, v88, v89
	v_cvt_pk_bf16_f32 v73, v92, v93
	v_cvt_pk_bf16_f32 v74, v90, v91
	v_cvt_pk_bf16_f32 v75, v94, v95
	v_add_u32_e32 v161, s14, v152
	s_waitcnt lgkmcnt(6)
	v_mfma_f32_32x32x16_bf16 v[48:63], v[224:227], v[76:79], v[48:63]
	v_cvt_pk_bf16_f32 v66, v66, v67
	v_cvt_pk_bf16_f32 v67, v70, v71
	v_cvt_pk_bf16_f32 v71, v166, v167
	v_add_u32_e32 v166, s14, v153
	v_cvt_pk_bf16_f32 v69, v164, v165
	v_cvt_pk_bf16_f32 v70, v162, v163
	v_add_u32_e32 v167, s14, v154
	ds_read_b64_tr_b16 v[162:163], v166
	ds_read_b64_tr_b16 v[164:165], v167 offset:768
	ds_read_b64_tr_b16 v[176:177], v166 offset:6144
	ds_read_b64_tr_b16 v[178:179], v167 offset:6912
	ds_read_b64_tr_b16 v[204:205], v166 offset:12288
	ds_read_b64_tr_b16 v[206:207], v167 offset:13056
	ds_read_b64_tr_b16 v[208:209], v166 offset:18432
	ds_read_b64_tr_b16 v[210:211], v167 offset:19200
	s_waitcnt lgkmcnt(12)
	v_mfma_f32_32x32x16_bf16 v[48:63], v[228:231], v[72:75], v[48:63]
	s_add_i32 s14, s10, -2
	s_and_b32 s14, s14, 3
	s_mulk_i32 s14, 0x6000
	s_waitcnt lgkmcnt(6)
	v_mfma_f32_32x32x16_bf16 v[32:47], v[162:165], v[76:79], v[32:47]
	v_mfma_f32_32x32x16_bf16 v[48:63], v[232:235], v[64:67], v[48:63]
	s_waitcnt lgkmcnt(4)
	v_mfma_f32_32x32x16_bf16 v[32:47], v[176:179], v[72:75], v[32:47]
	v_mfma_f32_32x32x16_bf16 v[48:63], v[236:239], v[68:71], v[48:63]
	ds_read_b64_tr_b16 v[80:81], v146 offset:128
	ds_read_b64_tr_b16 v[82:83], v161 offset:896
	ds_read_b64_tr_b16 v[92:93], v146 offset:6272
	ds_read_b64_tr_b16 v[94:95], v161 offset:7040
	ds_read_b64_tr_b16 v[212:213], v146 offset:12416
	ds_read_b64_tr_b16 v[214:215], v161 offset:13184
	ds_read_b64_tr_b16 v[88:89], v146 offset:18560
	ds_read_b64_tr_b16 v[90:91], v161 offset:19328
	v_add_u32_e32 v146, s14, v147
	v_add_u32_e32 v161, s14, v148
	s_waitcnt lgkmcnt(10)
	v_mfma_f32_32x32x16_bf16 v[32:47], v[204:207], v[64:67], v[32:47]
	ds_read_b64_tr_b16 v[84:85], v166 offset:128
	ds_read_b64_tr_b16 v[86:87], v167 offset:896
	ds_read_b64_tr_b16 v[162:163], v166 offset:6272
	ds_read_b64_tr_b16 v[164:165], v167 offset:7040
	ds_read_b64_tr_b16 v[176:177], v166 offset:12416
	ds_read_b64_tr_b16 v[178:179], v167 offset:13184
	ds_read_b64_tr_b16 v[204:205], v166 offset:18560
	ds_read_b64_tr_b16 v[206:207], v167 offset:19328
	v_add_u32_e32 v166, s14, v149
	v_add_u32_e32 v167, s14, v150
	s_waitcnt lgkmcnt(14)
	v_mfma_f32_32x32x16_bf16 v[0:15], v[80:83], v[76:79], v[0:15]
	s_waitcnt lgkmcnt(6)
	v_mfma_f32_32x32x16_bf16 v[16:31], v[84:87], v[76:79], v[16:31]
	v_mfma_f32_32x32x16_bf16 v[0:15], v[92:95], v[72:75], v[0:15]
	s_waitcnt lgkmcnt(4)
	v_mfma_f32_32x32x16_bf16 v[16:31], v[162:165], v[72:75], v[16:31]
	v_mfma_f32_32x32x16_bf16 v[0:15], v[212:215], v[64:67], v[0:15]
	s_waitcnt lgkmcnt(2)
	v_mfma_f32_32x32x16_bf16 v[16:31], v[176:179], v[64:67], v[16:31]
	v_mfma_f32_32x32x16_bf16 v[32:47], v[208:211], v[68:71], v[32:47]
	v_mfma_f32_32x32x16_bf16 v[0:15], v[88:91], v[68:71], v[0:15]
	s_waitcnt lgkmcnt(0)
	v_mfma_f32_32x32x16_bf16 v[16:31], v[204:207], v[68:71], v[16:31]
	ds_read_b128 v[64:67], v146
	ds_read_b128 v[68:71], v146 offset:12288
	ds_read_b128 v[162:165], v161
	ds_read_b128 v[176:179], v161 offset:12288
	ds_read_b128 v[204:207], v166
	ds_read_b128 v[208:211], v166 offset:12288
	ds_read_b128 v[212:215], v167
	ds_read_b128 v[216:219], v167 offset:12288
	s_waitcnt lgkmcnt(6)
	v_mfma_f32_32x32x16_bf16 v[80:95], v[64:67], v[112:115], 0
	v_mfma_f32_32x32x16_bf16 v[64:79], v[68:71], v[112:115], 0
	s_waitcnt lgkmcnt(4)
	v_mfma_f32_32x32x16_bf16 v[80:95], v[162:165], v[116:119], v[80:95]
	ds_read_b128 v[162:165], v146 offset:128
	ds_read_b128 v[220:223], v146 offset:12416
	v_mfma_f32_32x32x16_bf16 v[64:79], v[176:179], v[116:119], v[64:79]
	s_waitcnt lgkmcnt(4)
	v_mfma_f32_32x32x16_bf16 v[80:95], v[204:207], v[120:123], v[80:95]
	ds_read_b128 v[176:179], v161 offset:128
	ds_read_b128 v[204:207], v161 offset:12416
	v_mfma_f32_32x32x16_bf16 v[64:79], v[208:211], v[120:123], v[64:79]
	s_waitcnt lgkmcnt(4)
	v_mfma_f32_32x32x16_bf16 v[80:95], v[212:215], v[124:127], v[80:95]
	ds_read_b128 v[208:211], v166 offset:128
	ds_read_b128 v[212:215], v166 offset:12416
	v_mfma_f32_32x32x16_bf16 v[64:79], v[216:219], v[124:127], v[64:79]
	s_waitcnt lgkmcnt(4)
	v_mfma_f32_32x32x16_bf16 v[80:95], v[162:165], v[96:99], v[80:95]
	ds_read_b128 v[162:165], v167 offset:128
	ds_read_b128 v[216:219], v167 offset:12416
	v_mfma_f32_32x32x16_bf16 v[64:79], v[220:223], v[96:99], v[64:79]
	s_waitcnt lgkmcnt(4)
	v_mfma_f32_32x32x16_bf16 v[80:95], v[176:179], v[100:103], v[80:95]
	ds_read_b128 v[176:179], v146 offset:256
	ds_read_b128 v[220:223], v146 offset:12544
	v_mfma_f32_32x32x16_bf16 v[64:79], v[204:207], v[100:103], v[64:79]
	s_waitcnt lgkmcnt(4)
	v_mfma_f32_32x32x16_bf16 v[80:95], v[208:211], v[104:107], v[80:95]
	ds_read_b128 v[204:207], v161 offset:256
	ds_read_b128 v[208:211], v161 offset:12544
	v_mfma_f32_32x32x16_bf16 v[64:79], v[212:215], v[104:107], v[64:79]
	s_waitcnt lgkmcnt(4)
	v_mfma_f32_32x32x16_bf16 v[80:95], v[162:165], v[108:111], v[80:95]
	ds_read_b128 v[162:165], v166 offset:256
	ds_read_b128 v[212:215], v166 offset:12544
	v_mfma_f32_32x32x16_bf16 v[64:79], v[216:219], v[108:111], v[64:79]
	s_waitcnt lgkmcnt(4)
	v_mfma_f32_32x32x16_bf16 v[80:95], v[176:179], v[128:131], v[80:95]
	ds_read_b128 v[176:179], v167 offset:256
	ds_read_b128 v[216:219], v167 offset:12544
	v_mfma_f32_32x32x16_bf16 v[64:79], v[220:223], v[128:131], v[64:79]
	s_waitcnt lgkmcnt(4)
	v_mfma_f32_32x32x16_bf16 v[80:95], v[204:207], v[132:135], v[80:95]
	v_mfma_f32_32x32x16_bf16 v[64:79], v[208:211], v[132:135], v[64:79]
	s_waitcnt lgkmcnt(2)
	v_mfma_f32_32x32x16_bf16 v[80:95], v[162:165], v[136:139], v[80:95]
	v_mfma_f32_32x32x16_bf16 v[64:79], v[212:215], v[136:139], v[64:79]
	s_waitcnt lgkmcnt(0)
	v_mfma_f32_32x32x16_bf16 v[80:95], v[176:179], v[140:143], v[80:95]
	v_mfma_f32_32x32x16_bf16 v[64:79], v[216:219], v[140:143], v[64:79]
	s_cmp_le_u32 s7, s44
	s_cbranch_scc1 .Lf_b
	v_add_u32_e32 v146, 59, v156
	v_cmp_le_i32_e64 s[16:17], 0, v146
	v_cmp_le_i32_e64 s[18:19], 32, v146
	v_cmp_le_i32_e64 vcc, 1, v146
	s_nop 4
	v_cndmask_b32_e64 v80, v199, v80, s[16:17]
	v_cmp_le_i32_e64 s[16:17], 33, v146
	v_cndmask_b32_e64 v64, v199, v64, s[18:19]
	v_cmp_le_i32_e64 s[18:19], 2, v146
	v_cndmask_b32_e64 v81, v199, v81, vcc
	v_cmp_le_i32_e64 vcc, 34, v146
	v_cndmask_b32_e64 v65, v199, v65, s[16:17]
	v_cmp_le_i32_e64 s[16:17], 3, v146
	v_cndmask_b32_e64 v82, v199, v82, s[18:19]
	v_cmp_le_i32_e64 s[18:19], 35, v146
	v_cndmask_b32_e64 v66, v199, v66, vcc
	v_cmp_le_i32_e64 vcc, 8, v146
	v_cndmask_b32_e64 v83, v199, v83, s[16:17]
	v_cmp_le_i32_e64 s[16:17], 40, v146
	v_cndmask_b32_e64 v67, v199, v67, s[18:19]
	v_cmp_le_i32_e64 s[18:19], 9, v146
	v_cndmask_b32_e64 v84, v199, v84, vcc
	v_cmp_le_i32_e64 vcc, 41, v146
	v_cndmask_b32_e64 v68, v199, v68, s[16:17]
	v_cmp_le_i32_e64 s[16:17], 10, v146
	v_cndmask_b32_e64 v85, v199, v85, s[18:19]
	v_cmp_le_i32_e64 s[18:19], 42, v146
	v_cndmask_b32_e64 v69, v199, v69, vcc
	v_cmp_le_i32_e64 vcc, 11, v146
	v_cndmask_b32_e64 v86, v199, v86, s[16:17]
	v_cmp_le_i32_e64 s[16:17], 43, v146
	v_cndmask_b32_e64 v70, v199, v70, s[18:19]
	v_cmp_le_i32_e64 s[18:19], 16, v146
	v_cndmask_b32_e64 v87, v199, v87, vcc
	v_cmp_le_i32_e64 vcc, 48, v146
	v_cndmask_b32_e64 v71, v199, v71, s[16:17]
	v_cmp_le_i32_e64 s[16:17], 17, v146
	v_cndmask_b32_e64 v88, v199, v88, s[18:19]
	v_cmp_le_i32_e64 s[18:19], 49, v146
	v_cndmask_b32_e64 v72, v199, v72, vcc
	v_cmp_le_i32_e64 vcc, 18, v146
	v_cndmask_b32_e64 v89, v199, v89, s[16:17]
	v_cmp_le_i32_e64 s[16:17], 50, v146
	v_cndmask_b32_e64 v73, v199, v73, s[18:19]
	v_cmp_le_i32_e64 s[18:19], 19, v146
	v_cndmask_b32_e64 v90, v199, v90, vcc
	v_cmp_le_i32_e64 vcc, 51, v146
	v_cndmask_b32_e64 v74, v199, v74, s[16:17]
	v_cmp_le_i32_e64 s[16:17], 24, v146
	v_cndmask_b32_e64 v91, v199, v91, s[18:19]
	v_cmp_le_i32_e64 s[18:19], 56, v146
	v_cndmask_b32_e64 v75, v199, v75, vcc
	v_cmp_le_i32_e64 vcc, 25, v146
	v_cndmask_b32_e64 v92, v199, v92, s[16:17]
	v_cmp_le_i32_e64 s[16:17], 57, v146
	v_cndmask_b32_e64 v76, v199, v76, s[18:19]
	v_cmp_le_i32_e64 s[18:19], 26, v146
	v_cndmask_b32_e64 v93, v199, v93, vcc
	v_cmp_le_i32_e64 vcc, 58, v146
	v_cndmask_b32_e64 v77, v199, v77, s[16:17]
	v_cmp_le_i32_e64 s[16:17], 27, v146
	v_cndmask_b32_e64 v94, v199, v94, s[18:19]
	v_cmp_le_i32_e64 s[18:19], 59, v146
	v_cndmask_b32_e64 v78, v199, v78, vcc
	v_cndmask_b32_e64 v95, v199, v95, s[16:17]
	v_cndmask_b32_e64 v79, v199, v79, s[18:19]
